# HGRN2 pass A items dealt from a queue word so late-arriving workgroups skip them (on top of v12)
# speedup vs baseline: 1.0081x; 1.0081x over previous
.LBB0_1367:
	s_mov_b64 s[6:7], s[0:1]
	s_barrier
	s_load_dwordx2 s[100:101], s[0:1], 0x90
	s_waitcnt lgkmcnt(0)
	s_add_u32 s100, s100, 0x8080
	s_addc_u32 s101, s101, 0
	v_cmp_eq_u32_e64 s[98:99], 0, v0
	s_and_saveexec_b64 s[98:99], s[98:99]
	s_cbranch_execz .Lpaq_fa
	v_mov_b32_e32 v240, 1
	v_mov_b32_e32 v241, 0
	global_atomic_add v240, v241, v240, s[100:101] sc0
	v_mov_b32_e32 v242, 0x24100
	s_waitcnt vmcnt(0)
	ds_write_b32 v242, v240
	s_waitcnt lgkmcnt(0)
.Lpaq_fa:
	s_or_b64 exec, exec, s[98:99]
	s_barrier
	v_mov_b32_e32 v242, 0x24100
	ds_read_b32 v240, v242
	s_waitcnt lgkmcnt(0)
	v_readfirstlane_b32 s54, v240
	s_mov_b64 s[6:7], s[0:1]
	s_mov_b64 s[8:9], s[0:1]
	s_mov_b64 s[10:11], s[0:1]
	s_mov_b64 s[12:13], s[0:1]
	v_mov_b32_e32 v2, v0
	s_cmpk_gt_i32 s54, 0xef
	v_readfirstlane_b32 s24, v2
	s_cbranch_scc1 .LBB0_1386
	s_load_dwordx2 s[14:15], s[6:7], 0x90
	s_load_dwordx2 s[16:17], s[8:9], 0x90
	s_load_dwordx2 s[18:19], s[10:11], 0x90
	s_load_dwordx2 s[34:35], s[12:13], 0x90
	v_ashrrev_i32_e32 v6, 3, v2
	s_waitcnt lgkmcnt(0)
	s_add_u32 s28, s14, 0x28400000
	s_addc_u32 s29, s15, 0
	s_add_u32 s30, s16, 0x2c400000
	v_and_b32_e32 v6, -8, v6
	s_addc_u32 s31, s17, 0
	v_lshlrev_b32_e32 v4, 1, v2
	v_ashrrev_i32_e32 v7, 31, v6
	s_add_u32 s3, s18, 0x30400000
	v_and_b32_e32 v5, 0x7e, v4
	v_lshlrev_b64 v[50:51], 7, v[6:7]
	s_movk_i32 s25, 0x90
	v_and_b32_e32 v3, 63, v2
	s_addc_u32 s42, s19, 0
	v_or_b32_e32 v50, v50, v5
	s_add_i32 s6, 0, 0x1c400
	v_lshlrev_b32_e32 v7, 2, v5
	v_mad_u32_u24 v8, v5, s25, 0
	v_and_b32_e32 v5, 15, v2
	v_ashrrev_i32_e32 v6, 6, v2
	v_add_u32_e32 v64, s6, v7
	s_ashr_i32 s36, s24, 2
	v_mad_u32_u24 v68, v5, s25, 0
	v_or_b32_e32 v5, 48, v3
	v_lshl_add_u32 v65, v6, 9, v64
	v_cmp_lt_i32_e64 s[8:9], 7, v6
	v_cmp_lt_i32_e64 s[10:11], 6, v6
	v_cmp_lt_i32_e64 s[12:13], 5, v6
	v_cmp_lt_i32_e64 s[14:15], 4, v6
	v_cmp_lt_i32_e64 s[16:17], 3, v6
	v_cmp_lt_i32_e64 s[18:19], 2, v6
	v_cmp_lt_i32_e64 s[20:21], 1, v6
	v_cmp_lt_i32_e64 s[22:23], 0, v6
	v_lshlrev_b32_e32 v9, 4, v6
	s_and_b32 s37, s36, -16
	v_bfi_b32 v6, -16, s36, v2
	v_mad_u32_u24 v12, v5, s25, 0
	v_or_b32_e32 v5, 0x70, v3
	s_andn2_b32 s24, s24, 63
	s_add_i32 s38, 0, 0x1d400
	s_lshl_b32 s37, s37, 2
	v_mul_lo_u32 v6, v6, s25
	v_mad_u32_u24 v13, v5, s25, 0
	s_ashr_i32 s25, s24, 31
	v_ashrrev_i32_e32 v5, 31, v4
	v_cmp_gt_u32_e64 s[6:7], 64, v2
	s_add_i32 s37, s38, s37
	v_and_b32_e32 v66, 48, v2
	v_add_u32_e32 v10, 0, v6
	v_add_u32_e32 v11, 0xd000, v68
	v_add_u32_e32 v69, s38, v7
	v_or_b32_e32 v6, s24, v3
	v_mov_b32_e32 v7, s25
	v_cmp_gt_i32_e64 s[24:25], 64, v2
	v_lshl_add_u64 v[2:3], v[4:5], 2, s[34:35]
	s_mov_b64 s[34:35], 0x32400000
	v_add_u32_e32 v67, s37, v66
	v_lshl_add_u64 v[52:53], v[2:3], 0, s[34:35]
	v_lshlrev_b64 v[54:55], 4, v[6:7]
	s_movk_i32 s43, 0x7fff
	s_mov_b32 s52, 0xffff0000
	s_mov_b32 s53, 0xffff
	v_add_u32_e32 v70, v8, v9
	v_add_u32_e32 v71, v10, v66
	v_add_u32_e32 v72, v12, v66
	v_add_u32_e32 v73, v11, v66
	v_add_u32_e32 v74, v13, v66
	v_mov_b32_e32 v75, 1
	s_branch .LBB0_1370
.LBB0_1369:
	s_or_b64 exec, exec, s[36:37]
	v_cmp_eq_u32_e64 s[98:99], 0, v0
	s_and_saveexec_b64 s[98:99], s[98:99]
	s_cbranch_execz .Lpaq_fb
	v_mov_b32_e32 v240, 1
	v_mov_b32_e32 v241, 0
	global_atomic_add v240, v241, v240, s[100:101] sc0
	v_mov_b32_e32 v242, 0x24100
	s_waitcnt vmcnt(0)
	ds_write_b32 v242, v240
	s_waitcnt lgkmcnt(0)
.Lpaq_fb:
	s_or_b64 exec, exec, s[98:99]
	s_barrier
	v_mov_b32_e32 v242, 0x24100
	ds_read_b32 v240, v242
	s_waitcnt lgkmcnt(0)
	v_readfirstlane_b32 s54, v240
	s_cmpk_lt_i32 s54, 0xf0
	s_cbranch_scc0 .LBB0_1386
